# prep declared with 72 VGPRs so at most one 16-wave workgroup per CU (even spread of the 256 working blocks); otherwise v23
# baseline (speedup 1.0000x reference)
	.amdhsa_kernel _Z11prep_kernelPKfS0_S0_S0_Pf
		.amdhsa_group_segment_fixed_size 2112
		.amdhsa_private_segment_fixed_size 0
		.amdhsa_kernarg_size 40
		.amdhsa_user_sgpr_count 2
		.amdhsa_user_sgpr_dispatch_ptr 0
		.amdhsa_user_sgpr_queue_ptr 0
		.amdhsa_user_sgpr_kernarg_segment_ptr 1
		.amdhsa_user_sgpr_dispatch_id 0
		.amdhsa_user_sgpr_kernarg_preload_length 0
		.amdhsa_user_sgpr_kernarg_preload_offset 0
		.amdhsa_user_sgpr_private_segment_size 0
		.amdhsa_uses_dynamic_stack 0
		.amdhsa_enable_private_segment 0
		.amdhsa_system_sgpr_workgroup_id_x 1
		.amdhsa_system_sgpr_workgroup_id_y 0
		.amdhsa_system_sgpr_workgroup_id_z 0
		.amdhsa_system_sgpr_workgroup_info 0
		.amdhsa_system_vgpr_workitem_id 0
		.amdhsa_next_free_vgpr 72
		.amdhsa_next_free_sgpr 26
		.amdhsa_accum_offset 72
		.amdhsa_reserve_vcc 1
		.amdhsa_float_round_mode_32 0
		.amdhsa_float_round_mode_16_64 0
		.amdhsa_float_denorm_mode_32 3
		.amdhsa_float_denorm_mode_16_64 3
		.amdhsa_dx10_clamp 1
		.amdhsa_ieee_mode 1
		.amdhsa_fp16_overflow 0
		.amdhsa_tg_split 0
		.amdhsa_exception_fp_ieee_invalid_op 0
		.amdhsa_exception_fp_denorm_src 0
		.amdhsa_exception_fp_ieee_div_zero 0
		.amdhsa_exception_fp_ieee_overflow 0
		.amdhsa_exception_fp_ieee_underflow 0
		.amdhsa_exception_fp_ieee_inexact 0
		.amdhsa_exception_int_div_zero 0
	.end_amdhsa_kernel

.Lfunc_end0:
	.size	_Z11prep_kernelPKfS0_S0_S0_Pf, .Lfunc_end0-_Z11prep_kernelPKfS0_S0_S0_Pf
	.set _Z11prep_kernelPKfS0_S0_S0_Pf.num_vgpr, 72
	.set _Z11prep_kernelPKfS0_S0_S0_Pf.num_agpr, 0
	.set _Z11prep_kernelPKfS0_S0_S0_Pf.numbered_sgpr, 26
	.set _Z11prep_kernelPKfS0_S0_S0_Pf.num_named_barrier, 0
	.set _Z11prep_kernelPKfS0_S0_S0_Pf.private_seg_size, 0
	.set _Z11prep_kernelPKfS0_S0_S0_Pf.uses_vcc, 1
	.set _Z11prep_kernelPKfS0_S0_S0_Pf.uses_flat_scratch, 0
	.set _Z11prep_kernelPKfS0_S0_S0_Pf.has_dyn_sized_stack, 0
	.set _Z11prep_kernelPKfS0_S0_S0_Pf.has_recursion, 0
	.set _Z11prep_kernelPKfS0_S0_S0_Pf.has_indirect_call, 0

amdhsa.kernels:
  - .agpr_count:     0
    .args:
      - .actual_access:  read_only
        .address_space:  global
        .offset:         0
        .size:           8
        .value_kind:     global_buffer
      - .actual_access:  read_only
        .address_space:  global
        .offset:         8
        .size:           8
        .value_kind:     global_buffer
      - .actual_access:  read_only
        .address_space:  global
        .offset:         16
        .size:           8
        .value_kind:     global_buffer
      - .actual_access:  read_only
        .address_space:  global
        .offset:         24
        .size:           8
        .value_kind:     global_buffer
      - .actual_access:  write_only
        .address_space:  global
        .offset:         32
        .size:           8
        .value_kind:     global_buffer
    .group_segment_fixed_size: 2112
    .kernarg_segment_align: 8
    .kernarg_segment_size: 40
    .language:       OpenCL C
    .language_version:
      - 2
      - 0
    .max_flat_workgroup_size: 1024
    .name:           _Z11prep_kernelPKfS0_S0_S0_Pf
    .private_segment_fixed_size: 0
    .sgpr_count:     32
    .sgpr_spill_count: 0
    .symbol:         _Z11prep_kernelPKfS0_S0_S0_Pf.kd
    .uniform_work_group_size: 1
    .uses_dynamic_stack: false
    .vgpr_count:     72
    .vgpr_spill_count: 0
    .wavefront_size: 64
  - .agpr_count:     0
    .args:
      - .actual_access:  read_only
        .address_space:  global
        .offset:         0
        .size:           8
        .value_kind:     global_buffer
      - .address_space:  global
        .offset:         8
        .size:           8
        .value_kind:     global_buffer
    .group_segment_fixed_size: 4096
    .kernarg_segment_align: 8
    .kernarg_segment_size: 16
    .language:       OpenCL C
    .language_version:
      - 2
      - 0
    .max_flat_workgroup_size: 1024
    .name:           _Z13stream_kernelPKfPf
    .private_segment_fixed_size: 0
    .sgpr_count:     17
    .sgpr_spill_count: 0
    .symbol:         _Z13stream_kernelPKfPf.kd
    .uniform_work_group_size: 1
    .uses_dynamic_stack: false
    .vgpr_count:     67
    .vgpr_spill_count: 0
    .wavefront_size: 64
  - .agpr_count:     0
    .args:
      - .actual_access:  read_only
        .address_space:  global
        .offset:         0
        .size:           8
        .value_kind:     global_buffer
      - .actual_access:  write_only
        .address_space:  global
        .offset:         8
        .size:           8
        .value_kind:     global_buffer
    .group_segment_fixed_size: 32
    .kernarg_segment_align: 8
    .kernarg_segment_size: 16
    .language:       OpenCL C
    .language_version:
      - 2
      - 0
    .max_flat_workgroup_size: 256
    .name:           _Z14softmax_kernelPKfPf
    .private_segment_fixed_size: 0
    .sgpr_count:     16
    .sgpr_spill_count: 0
    .symbol:         _Z14softmax_kernelPKfPf.kd
    .uniform_work_group_size: 1
    .uses_dynamic_stack: false
    .vgpr_count:     17
    .vgpr_spill_count: 0
    .wavefront_size: 64
